# L1: first task peeled (static task=wave id, rowptr/index loads issued under the LDS staging, single barrier)
# speedup vs baseline: 1.0255x; 1.0050x over previous
_Z7k_layerILi1EEvPKDF16_PKiPKjS3_S3_S1_PKfPDF16_PhS3_S7_Pf:
	s_load_dwordx2 s[24:25], s[0:1], 0x50
	s_load_dwordx8 s[8:15], s[0:1], 0x0
	s_load_dwordx8 s[16:23], s[0:1], 0x20
	v_lshrrev_b32_e32 v2, 5, v0
	v_and_b32_e32 v4, 31, v0
	v_mul_u32_u24_e32 v3, 0x210, v2
	v_lshlrev_b32_e32 v5, 4, v4
	v_or_b32_e32 v1, 0xfffffc00, v0
	v_add3_u32 v4, v3, v5, 0
	v_lshl_or_b32 v2, v2, 9, v5
	v_mov_b32_e32 v3, 0
	s_waitcnt lgkmcnt(0)
	v_add_u32_e32 v3, 0x4000, v2
	v_lshlrev_b32_e32 v30, 4, v0
	v_cmp_gt_u32_e64 s[34:35], 16, v0
	v_lshrrev_b32_e32 v39, 6, v0
	s_and_saveexec_b64 s[4:5], s[34:35]
	global_load_dwordx4 v[42:45], v30, s[20:21]
	s_mov_b64 exec, s[4:5]
	global_load_dwordx4 v[6:9], v2, s[18:19]
	global_load_dwordx4 v[10:13], v3, s[18:19]
	v_add_u32_e32 v31, 0x4000, v30
	v_add_u32_e32 v32, 0x8000, v30
	v_add_u32_e32 v33, 0xc000, v30
	global_load_dwordx4 v[14:17], v30, s[8:9]
	global_load_dwordx4 v[18:21], v31, s[8:9]
	global_load_dwordx4 v[22:25], v32, s[8:9]
	global_load_dwordx4 v[26:29], v33, s[8:9]
	v_readfirstlane_b32 s36, v39
	v_mov_b32_e32 v40, v4
	v_add_u32_e32 v41, 0xcc10, v30
	v_add_u32_e32 v38, 0x1cc90, v30
	v_cmp_gt_u32_e32 vcc, 64, v0
	s_and_saveexec_b64 s[4:5], vcc
	v_lshl_add_u32 v1, v0, 1, 0
	v_add_u32_e32 v1, 0x1cc10, v1
	v_mov_b32_e32 v2, 0
	ds_write_b16 v1, v2
	s_mov_b64 exec, s[4:5]
	v_cmp_eq_u32_e32 vcc, 0, v0
	s_and_saveexec_b64 s[4:5], vcc
	v_mov_b32_e32 v1, 0
	v_mov_b32_e32 v2, 16
	ds_write_b32 v1, v2 offset:52224
	s_mov_b64 exec, s[4:5]
	s_mul_i32 s8, s2, 0x186a0
	s_lshr_b32 s8, s8, 8
	s_add_i32 s3, s2, 1
	s_mul_i32 s18, s3, 0x186a0
	s_lshr_b32 s18, s18, 8
.LBB4_14:
	v_lshrrev_b32_e32 v2, 3, v0
	s_load_dwordx2 s[4:5], s[0:1], 0x40
	v_and_b32_e32 v2, 0x78, v2
	s_movk_i32 s2, 0x90
	v_and_b32_e32 v97, 7, v0
	s_sub_i32 s0, s18, s8
	v_and_b32_e32 v1, 63, v0
	v_mov_b32_e32 v89, 0
	v_mad_u32_u24 v3, v2, s2, 0
	v_bfe_u32 v96, v0, 3, 3
	v_and_b32_e32 v99, 15, v0
	v_bfe_u32 v4, v0, 4, 2
	s_add_i32 s0, s0, 7
	v_mul_u32_u24_e32 v5, 0x90, v97
	v_and_b32_e32 v0, 48, v0
	s_ashr_i32 s9, s0, 3
	v_cmp_eq_u32_e64 s[0:1], 0, v1
	v_mad_u32_u24 v1, v96, s2, v3
	v_lshlrev_b32_e32 v2, 3, v4
	v_add3_u32 v103, v3, v5, v0
	v_mov_b32_e32 v3, v89
	v_lshlrev_b32_e32 v98, 4, v97
	v_add_u32_e32 v0, 0, v0
	v_lshlrev_b32_e32 v88, 2, v4
	v_lshl_add_u64 v[90:91], s[22:23], 0, v[2:3]
	v_mul_u32_u24_e32 v2, 0x210, v99
	v_or_b32_e32 v100, 8, v97
	v_or_b32_e32 v101, 16, v97
	v_add_u32_e32 v102, 0, v98
	v_cmp_gt_u32_e64 s[2:3], 8, v99
	s_waitcnt lgkmcnt(0)
	v_lshl_add_u64 v[92:93], s[4:5], 0, v[88:89]
	v_lshlrev_b32_e32 v88, 2, v88
	v_add_u32_e32 v104, v1, v98
	v_add_u32_e32 v105, v0, v2
	s_lshl_b32 s19, s36, 3
	s_add_i32 s19, s19, s8
	v_add_u32_e32 v94, s19, v96
	v_cmp_gt_i32_e64 s[4:5], s18, v94
	v_mov_b32_e32 v32, 0
	v_mov_b32_e32 v33, 0
	v_mov_b32_e32 v34, 0
	v_mov_b32_e32 v35, 0
	s_and_saveexec_b64 s[6:7], s[4:5]
	v_lshl_add_u32 v36, v94, 1, v94
	v_lshlrev_b32_e32 v36, 2, v36
	global_load_dwordx4 v[32:35], v36, s[10:11]
	s_mov_b64 exec, s[6:7]
	s_waitcnt vmcnt(6)
	ds_write_b128 v40, v[6:9]
	s_waitcnt vmcnt(5)
	ds_write_b128 v40, v[10:13] offset:16896
	s_waitcnt vmcnt(4)
	ds_write_b128 v41, v[14:17]
	s_waitcnt vmcnt(3)
	ds_write_b128 v41, v[18:21] offset:16384
	s_waitcnt vmcnt(2)
	ds_write_b128 v41, v[22:25] offset:32768
	s_waitcnt vmcnt(1)
	ds_write_b128 v41, v[26:29] offset:49152
	s_and_saveexec_b64 s[6:7], s[34:35]
	ds_write_b128 v38, v[42:45]
	s_mov_b64 exec, s[6:7]
	s_waitcnt vmcnt(0)
	v_sub_u32_e32 v72, v33, v32
	v_sub_u32_e32 v108, v34, v33
	v_sub_u32_e32 v35, v35, v34
	v_add_lshl_u32 v37, v32, v97, 2
	v_add_lshl_u32 v38, v33, v97, 2
	v_add_lshl_u32 v39, v34, v97, 2
	v_mov_b32_e32 v36, 0x4000000
	v_mov_b32_e32 v68, 0x4000000
	v_mov_b32_e32 v74, 0x4000000
	v_mov_b32_e32 v85, 0x4000000
	v_mov_b32_e32 v84, 0x4000000
	v_mov_b32_e32 v109, 0x4000000
	v_mov_b32_e32 v107, 0x4000000
	v_mov_b32_e32 v106, 0x4000000
	v_mov_b32_e32 v95, 0x4000000
	s_mov_b64 s[6:7], exec
	v_cmp_lt_i32_e32 vcc, v97, v72
	s_and_b64 exec, exec, vcc
	global_load_dword v36, v37, s[12:13]
	v_cmp_lt_i32_e32 vcc, v100, v72
	s_and_b64 exec, exec, vcc
	global_load_dword v68, v37, s[12:13] offset:32
	v_cmp_lt_i32_e32 vcc, v101, v72
	s_and_b64 exec, exec, vcc
	global_load_dword v74, v37, s[12:13] offset:64
	s_mov_b64 exec, s[6:7]
	v_cmp_lt_i32_e32 vcc, v97, v108
	s_and_b64 exec, exec, vcc
	global_load_dword v85, v38, s[12:13]
	v_cmp_lt_i32_e32 vcc, v100, v108
	s_and_b64 exec, exec, vcc
	global_load_dword v84, v38, s[12:13] offset:32
	v_cmp_lt_i32_e32 vcc, v101, v108
	s_and_b64 exec, exec, vcc
	global_load_dword v109, v38, s[12:13] offset:64
	s_mov_b64 exec, s[6:7]
	v_cmp_lt_i32_e32 vcc, v97, v35
	s_and_b64 exec, exec, vcc
	global_load_dword v107, v39, s[12:13]
	v_cmp_lt_i32_e32 vcc, v100, v35
	s_and_b64 exec, exec, vcc
	global_load_dword v106, v39, s[12:13] offset:32
	v_cmp_lt_i32_e32 vcc, v101, v35
	s_and_b64 exec, exec, vcc
	global_load_dword v95, v39, s[12:13] offset:64
	s_mov_b64 exec, s[6:7]
	s_waitcnt lgkmcnt(0)
	s_barrier
	s_cmp_ge_i32 s36, s9
	s_cbranch_scc1 .LBB4_103
	s_branch .Lp1_after_idx

.Lp1_after_idx:
	s_waitcnt vmcnt(0)
	v_lshrrev_b32_e32 v36, 10, v36
	v_lshrrev_b32_e32 v68, 10, v68
	v_lshrrev_b32_e32 v74, 10, v74
	v_lshrrev_b32_e32 v85, 10, v85
	v_lshrrev_b32_e32 v84, 10, v84
	v_lshrrev_b32_e32 v109, 10, v109
	v_lshrrev_b32_e32 v107, 10, v107
	v_lshrrev_b32_e32 v106, 10, v106
	v_lshrrev_b32_e32 v95, 10, v95
	v_and_b32_e32 v36, 0x3fff80, v36
	v_and_b32_e32 v68, 0x3fff80, v68
	v_and_b32_e32 v74, 0x3fff80, v74
	v_and_b32_e32 v85, 0x3fff80, v85
	v_and_b32_e32 v84, 0x3fff80, v84
	v_and_b32_e32 v109, 0x3fff80, v109
	v_and_b32_e32 v107, 0x3fff80, v107
	v_and_b32_e32 v106, 0x3fff80, v106
	v_and_b32_e32 v95, 0x3fff80, v95
	ds_swizzle_b32 v37, v36 offset:swizzle(BROADCAST,8,0)
	ds_swizzle_b32 v38, v36 offset:swizzle(BROADCAST,8,1)
	ds_swizzle_b32 v39, v36 offset:swizzle(BROADCAST,8,2)
	ds_swizzle_b32 v40, v36 offset:swizzle(BROADCAST,8,3)
	ds_swizzle_b32 v41, v36 offset:swizzle(BROADCAST,8,6)
	s_waitcnt lgkmcnt(4)
	v_add_u32_e32 v37, v102, v37
	s_waitcnt lgkmcnt(3)
	v_add_u32_e32 v38, v102, v38
	ds_read_b128 v[60:63], v37 offset:52240
	ds_read_b128 v[52:55], v38 offset:52240
	s_waitcnt lgkmcnt(4)
	v_add_u32_e32 v37, v102, v39
	ds_swizzle_b32 v38, v36 offset:swizzle(BROADCAST,8,4)
	s_waitcnt lgkmcnt(4)
	v_add_u32_e32 v39, v102, v40
	ds_swizzle_b32 v40, v36 offset:swizzle(BROADCAST,8,5)
	ds_swizzle_b32 v42, v36 offset:swizzle(BROADCAST,8,7)
	ds_read_b128 v[64:67], v37 offset:52240
	ds_read_b128 v[56:59], v39 offset:52240
	s_waitcnt lgkmcnt(4)
	v_add_u32_e32 v37, v102, v38
	v_cmp_lt_i32_e32 vcc, 8, v72
	s_waitcnt lgkmcnt(3)
	v_add_u32_e32 v36, v102, v40
	v_add_u32_e32 v40, v102, v41
	s_waitcnt lgkmcnt(2)
	v_add_u32_e32 v41, v102, v42
	ds_read_b128 v[44:47], v37 offset:52240
	ds_read_b128 v[36:39], v36 offset:52240
	ds_read_b128 v[48:51], v40 offset:52240
	ds_read_b128 v[40:43], v41 offset:52240
	s_cmp_lg_u64 vcc, 0
	s_cselect_b64 s[22:23], -1, 0
	v_cmp_lt_i32_e64 s[6:7], 12, v72
	s_cbranch_vccz .LBB4_44
	ds_swizzle_b32 v0, v68 offset:swizzle(BROADCAST,8,0)
	ds_swizzle_b32 v1, v68 offset:swizzle(BROADCAST,8,1)
	ds_swizzle_b32 v16, v68 offset:swizzle(BROADCAST,8,2)
	ds_swizzle_b32 v17, v68 offset:swizzle(BROADCAST,8,3)
	s_waitcnt lgkmcnt(3)
	v_add_u32_e32 v0, v102, v0
	s_waitcnt lgkmcnt(2)
	v_add_u32_e32 v8, v102, v1
	s_waitcnt lgkmcnt(1)
	v_add_u32_e32 v16, v102, v16
	s_waitcnt lgkmcnt(0)
	v_add_u32_e32 v24, v102, v17
	ds_read_b128 v[0:3], v0 offset:52240
	ds_read_b128 v[8:11], v8 offset:52240
	ds_read_b128 v[16:19], v16 offset:52240
	ds_read_b128 v[24:27], v24 offset:52240

	.amdhsa_kernel _Z7k_layerILi1EEvPKDF16_PKiPKjS3_S3_S1_PKfPDF16_PhS3_S7_Pf
		.amdhsa_group_segment_fixed_size 256
		.amdhsa_private_segment_fixed_size 0
		.amdhsa_kernarg_size 352
		.amdhsa_user_sgpr_count 2
		.amdhsa_user_sgpr_dispatch_ptr 0
		.amdhsa_user_sgpr_queue_ptr 0
		.amdhsa_user_sgpr_kernarg_segment_ptr 1
		.amdhsa_user_sgpr_dispatch_id 0
		.amdhsa_user_sgpr_kernarg_preload_length 0
		.amdhsa_user_sgpr_kernarg_preload_offset 0
		.amdhsa_user_sgpr_private_segment_size 0
		.amdhsa_uses_dynamic_stack 0
		.amdhsa_enable_private_segment 0
		.amdhsa_system_sgpr_workgroup_id_x 1
		.amdhsa_system_sgpr_workgroup_id_y 0
		.amdhsa_system_sgpr_workgroup_id_z 0
		.amdhsa_system_sgpr_workgroup_info 0
		.amdhsa_system_vgpr_workitem_id 0
		.amdhsa_next_free_vgpr 114
		.amdhsa_next_free_sgpr 37
		.amdhsa_accum_offset 116
		.amdhsa_reserve_vcc 1
		.amdhsa_float_round_mode_32 0
		.amdhsa_float_round_mode_16_64 0
		.amdhsa_float_denorm_mode_32 3
		.amdhsa_float_denorm_mode_16_64 3
		.amdhsa_dx10_clamp 1
		.amdhsa_ieee_mode 1
		.amdhsa_fp16_overflow 0
		.amdhsa_tg_split 0
		.amdhsa_exception_fp_ieee_invalid_op 0
		.amdhsa_exception_fp_denorm_src 0
		.amdhsa_exception_fp_ieee_div_zero 0
		.amdhsa_exception_fp_ieee_overflow 0
		.amdhsa_exception_fp_ieee_underflow 0
		.amdhsa_exception_fp_ieee_inexact 0
		.amdhsa_exception_int_div_zero 0
	.end_amdhsa_kernel

amdhsa.kernels:
  - .agpr_count:     0
    .args:
      - .actual_access:  read_only
        .address_space:  global
        .offset:         0
        .size:           8
        .value_kind:     global_buffer
      - .actual_access:  read_only
        .address_space:  global
        .offset:         8
        .size:           8
        .value_kind:     global_buffer
      - .actual_access:  read_only
        .address_space:  global
        .offset:         16
        .size:           8
        .value_kind:     global_buffer
      - .actual_access:  read_only
        .address_space:  global
        .offset:         24
        .size:           8
        .value_kind:     global_buffer
      - .actual_access:  read_only
        .address_space:  global
        .offset:         32
        .size:           8
        .value_kind:     global_buffer
      - .actual_access:  read_only
        .address_space:  global
        .offset:         40
        .size:           8
        .value_kind:     global_buffer
      - .actual_access:  read_only
        .address_space:  global
        .offset:         48
        .size:           8
        .value_kind:     global_buffer
      - .actual_access:  read_only
        .address_space:  global
        .offset:         56
        .size:           8
        .value_kind:     global_buffer
      - .actual_access:  read_only
        .address_space:  global
        .offset:         64
        .size:           8
        .value_kind:     global_buffer
      - .actual_access:  read_only
        .address_space:  global
        .offset:         72
        .size:           8
        .value_kind:     global_buffer
      - .actual_access:  read_only
        .address_space:  global
        .offset:         80
        .size:           8
        .value_kind:     global_buffer
      - .actual_access:  read_only
        .address_space:  global
        .offset:         88
        .size:           8
        .value_kind:     global_buffer
      - .actual_access:  write_only
        .address_space:  global
        .offset:         96
        .size:           8
        .value_kind:     global_buffer
      - .actual_access:  write_only
        .address_space:  global
        .offset:         104
        .size:           8
        .value_kind:     global_buffer
      - .actual_access:  write_only
        .address_space:  global
        .offset:         112
        .size:           8
        .value_kind:     global_buffer
      - .actual_access:  write_only
        .address_space:  global
        .offset:         120
        .size:           8
        .value_kind:     global_buffer
      - .actual_access:  write_only
        .address_space:  global
        .offset:         128
        .size:           8
        .value_kind:     global_buffer
      - .actual_access:  write_only
        .address_space:  global
        .offset:         136
        .size:           8
        .value_kind:     global_buffer
      - .actual_access:  write_only
        .address_space:  global
        .offset:         144
        .size:           8
        .value_kind:     global_buffer
      - .actual_access:  write_only
        .address_space:  global
        .offset:         152
        .size:           8
        .value_kind:     global_buffer
      - .actual_access:  write_only
        .address_space:  global
        .offset:         160
        .size:           8
        .value_kind:     global_buffer
    .group_segment_fixed_size: 0
    .kernarg_segment_align: 8
    .kernarg_segment_size: 168
    .language:       OpenCL C
    .language_version:
      - 2
      - 0
    .max_flat_workgroup_size: 1024
    .name:           _Z6k_prepPKiS0_PKfS2_S2_S2_S2_S2_S2_S2_S2_S2_PDF16_S3_S3_PfS4_S4_PjS3_S5_
    .private_segment_fixed_size: 0
    .sgpr_count:     27
    .sgpr_spill_count: 0
    .symbol:         _Z6k_prepPKiS0_PKfS2_S2_S2_S2_S2_S2_S2_S2_S2_PDF16_S3_S3_PfS4_S4_PjS3_S5_.kd
    .uniform_work_group_size: 1
    .uses_dynamic_stack: false
    .vgpr_count:     61
    .vgpr_spill_count: 0
    .wavefront_size: 64
  - .agpr_count:     0
    .args:
      - .actual_access:  read_only
        .address_space:  global
        .offset:         0
        .size:           8
        .value_kind:     global_buffer
      - .actual_access:  read_only
        .address_space:  global
        .offset:         8
        .size:           8
        .value_kind:     global_buffer
      - .actual_access:  read_only
        .address_space:  global
        .offset:         16
        .size:           8
        .value_kind:     global_buffer
      - .actual_access:  write_only
        .address_space:  global
        .offset:         24
        .size:           8
        .value_kind:     global_buffer
      - .actual_access:  write_only
        .address_space:  global
        .offset:         32
        .size:           8
        .value_kind:     global_buffer
      - .actual_access:  write_only
        .address_space:  global
        .offset:         40
        .size:           8
        .value_kind:     global_buffer
      - .actual_access:  read_only
        .address_space:  global
        .offset:         48
        .size:           8
        .value_kind:     global_buffer
      - .actual_access:  read_only
        .address_space:  global
        .offset:         56
        .size:           8
        .value_kind:     global_buffer
      - .actual_access:  read_only
        .address_space:  global
        .offset:         64
        .size:           8
        .value_kind:     global_buffer
      - .actual_access:  read_only
        .address_space:  global
        .offset:         72
        .size:           8
        .value_kind:     global_buffer
      - .actual_access:  read_only
        .address_space:  global
        .offset:         80
        .size:           8
        .value_kind:     global_buffer
      - .actual_access:  read_only
        .address_space:  global
        .offset:         88
        .size:           8
        .value_kind:     global_buffer
      - .actual_access:  read_only
        .address_space:  global
        .offset:         96
        .size:           8
        .value_kind:     global_buffer
      - .actual_access:  read_only
        .address_space:  global
        .offset:         104
        .size:           8
        .value_kind:     global_buffer
      - .actual_access:  read_only
        .address_space:  global
        .offset:         112
        .size:           8
        .value_kind:     global_buffer
      - .actual_access:  read_only
        .address_space:  global
        .offset:         120
        .size:           8
        .value_kind:     global_buffer
      - .actual_access:  read_only
        .address_space:  global
        .offset:         128
        .size:           8
        .value_kind:     global_buffer
      - .actual_access:  write_only
        .address_space:  global
        .offset:         136
        .size:           8
        .value_kind:     global_buffer
      - .actual_access:  write_only
        .address_space:  global
        .offset:         144
        .size:           8
        .value_kind:     global_buffer
      - .actual_access:  write_only
        .address_space:  global
        .offset:         152
        .size:           8
        .value_kind:     global_buffer
      - .actual_access:  write_only
        .address_space:  global
        .offset:         160
        .size:           8
        .value_kind:     global_buffer
      - .actual_access:  write_only
        .address_space:  global
        .offset:         168
        .size:           8
        .value_kind:     global_buffer
    .group_segment_fixed_size: 1696
    .kernarg_segment_align: 8
    .kernarg_segment_size: 176
    .language:       OpenCL C
    .language_version:
      - 2
      - 0
    .max_flat_workgroup_size: 1024
    .name:           _Z11k_localsortPKiS0_S0_PjPtPiPKjPKfS7_S7_S7_S7_S7_S7_S7_S7_S7_PDF16_S8_S8_PfS9_
    .private_segment_fixed_size: 0
    .sgpr_count:     71
    .sgpr_spill_count: 0
    .symbol:         _Z11k_localsortPKiS0_S0_PjPtPiPKjPKfS7_S7_S7_S7_S7_S7_S7_S7_S7_PDF16_S8_S8_PfS9_.kd
    .uniform_work_group_size: 1
    .uses_dynamic_stack: false
    .vgpr_count:     95
    .vgpr_spill_count: 0
    .wavefront_size: 64
  - .agpr_count:     0
    .args:
      - .actual_access:  read_only
        .address_space:  global
        .offset:         0
        .size:           8
        .value_kind:     global_buffer
      - .actual_access:  read_only
        .address_space:  global
        .offset:         8
        .size:           8
        .value_kind:     global_buffer
      - .actual_access:  read_only
        .address_space:  global
        .offset:         16
        .size:           8
        .value_kind:     global_buffer
      - .actual_access:  write_only
        .address_space:  global
        .offset:         24
        .size:           8
        .value_kind:     global_buffer
      - .actual_access:  write_only
        .address_space:  global
        .offset:         32
        .size:           8
        .value_kind:     global_buffer
    .group_segment_fixed_size: 54144
    .kernarg_segment_align: 8
    .kernarg_segment_size: 40
    .language:       OpenCL C
    .language_version:
      - 2
      - 0
    .max_flat_workgroup_size: 1024
    .name:           _Z12k_bucketsortPKjPKtPKiPiPj
    .private_segment_fixed_size: 0
    .sgpr_count:     70
    .sgpr_spill_count: 0
    .symbol:         _Z12k_bucketsortPKjPKtPKiPiPj.kd
    .uniform_work_group_size: 1
    .uses_dynamic_stack: false
    .vgpr_count:     59
    .vgpr_spill_count: 0
    .wavefront_size: 64
  - .agpr_count:     0
    .args:
      - .actual_access:  read_only
        .address_space:  global
        .offset:         0
        .size:           8
        .value_kind:     global_buffer
      - .actual_access:  read_only
        .address_space:  global
        .offset:         8
        .size:           8
        .value_kind:     global_buffer
      - .actual_access:  write_only
        .address_space:  global
        .offset:         16
        .size:           8
        .value_kind:     global_buffer
    .group_segment_fixed_size: 0
    .kernarg_segment_align: 8
    .kernarg_segment_size: 24
    .language:       OpenCL C
    .language_version:
      - 2
      - 0
    .max_flat_workgroup_size: 256
    .name:           _Z7k_finalPKfS0_Pf
    .private_segment_fixed_size: 0
    .sgpr_count:     14
    .sgpr_spill_count: 0
    .symbol:         _Z7k_finalPKfS0_Pf.kd
    .uniform_work_group_size: 1
    .uses_dynamic_stack: false
    .vgpr_count:     10
    .vgpr_spill_count: 0
    .wavefront_size: 64
  - .agpr_count:     0
    .args:
      - .actual_access:  read_only
        .address_space:  global
        .offset:         0
        .size:           8
        .value_kind:     global_buffer
      - .actual_access:  read_only
        .address_space:  global
        .offset:         8
        .size:           8
        .value_kind:     global_buffer
      - .actual_access:  read_only
        .address_space:  global
        .offset:         16
        .size:           8
        .value_kind:     global_buffer
      - .actual_access:  read_only
        .address_space:  global
        .offset:         24
        .size:           8
        .value_kind:     global_buffer
      - .actual_access:  read_only
        .address_space:  global
        .offset:         32
        .size:           8
        .value_kind:     global_buffer
      - .actual_access:  read_only
        .address_space:  global
        .offset:         40
        .size:           8
        .value_kind:     global_buffer
      - .address_space:  global
        .offset:         48
        .size:           8
        .value_kind:     global_buffer
      - .actual_access:  write_only
        .address_space:  global
        .offset:         56
        .size:           8
        .value_kind:     global_buffer
      - .address_space:  global
        .offset:         64
        .size:           8
        .value_kind:     global_buffer
      - .actual_access:  read_only
        .address_space:  global
        .offset:         72
        .size:           8
        .value_kind:     global_buffer
      - .address_space:  global
        .offset:         80
        .size:           8
        .value_kind:     global_buffer
      - .actual_access:  read_only
        .address_space:  global
        .offset:         88
        .size:           8
        .value_kind:     global_buffer
      - .offset:         96
        .size:           4
        .value_kind:     hidden_block_count_x
      - .offset:         100
        .size:           4
        .value_kind:     hidden_block_count_y
      - .offset:         104
        .size:           4
        .value_kind:     hidden_block_count_z
      - .offset:         108
        .size:           2
        .value_kind:     hidden_group_size_x
      - .offset:         110
        .size:           2
        .value_kind:     hidden_group_size_y
      - .offset:         112
        .size:           2
        .value_kind:     hidden_group_size_z
      - .offset:         114
        .size:           2
        .value_kind:     hidden_remainder_x
      - .offset:         116
        .size:           2
        .value_kind:     hidden_remainder_y
      - .offset:         118
        .size:           2
        .value_kind:     hidden_remainder_z
      - .offset:         136
        .size:           8
        .value_kind:     hidden_global_offset_x
      - .offset:         144
        .size:           8
        .value_kind:     hidden_global_offset_y
      - .offset:         152
        .size:           8
        .value_kind:     hidden_global_offset_z
      - .offset:         160
        .size:           2
        .value_kind:     hidden_grid_dims
      - .offset:         216
        .size:           4
        .value_kind:     hidden_dynamic_lds_size
    .group_segment_fixed_size: 256
    .kernarg_segment_align: 8
    .kernarg_segment_size: 352
    .language:       OpenCL C
    .language_version:
      - 2
      - 0
    .max_flat_workgroup_size: 1024
    .name:           _Z7k_layerILi1EEvPKDF16_PKiPKjS3_S3_S1_PKfPDF16_PhS3_S7_Pf
    .private_segment_fixed_size: 0
    .sgpr_count:     43
    .sgpr_spill_count: 0
    .symbol:         _Z7k_layerILi1EEvPKDF16_PKiPKjS3_S3_S1_PKfPDF16_PhS3_S7_Pf.kd
    .uniform_work_group_size: 1
    .uses_dynamic_stack: false
    .vgpr_count:     114
    .vgpr_spill_count: 0
    .wavefront_size: 64
  - .agpr_count:     0
    .args:
      - .actual_access:  read_only
        .address_space:  global
        .offset:         0
        .size:           8
        .value_kind:     global_buffer
      - .actual_access:  read_only
        .address_space:  global
        .offset:         8
        .size:           8
        .value_kind:     global_buffer
      - .actual_access:  read_only
        .address_space:  global
        .offset:         16
        .size:           8
        .value_kind:     global_buffer
      - .actual_access:  read_only
        .address_space:  global
        .offset:         24
        .size:           8
        .value_kind:     global_buffer
      - .actual_access:  read_only
        .address_space:  global
        .offset:         32
        .size:           8
        .value_kind:     global_buffer
      - .actual_access:  read_only
        .address_space:  global
        .offset:         40
        .size:           8
        .value_kind:     global_buffer
      - .address_space:  global
        .offset:         48
        .size:           8
        .value_kind:     global_buffer
      - .actual_access:  read_only
        .address_space:  global
        .offset:         56
        .size:           8
        .value_kind:     global_buffer
      - .address_space:  global
        .offset:         64
        .size:           8
        .value_kind:     global_buffer
      - .actual_access:  read_only
        .address_space:  global
        .offset:         72
        .size:           8
        .value_kind:     global_buffer
      - .address_space:  global
        .offset:         80
        .size:           8
        .value_kind:     global_buffer
      - .address_space:  global
        .offset:         88
        .size:           8
        .value_kind:     global_buffer
      - .offset:         96
        .size:           4
        .value_kind:     hidden_block_count_x
      - .offset:         100
        .size:           4
        .value_kind:     hidden_block_count_y
      - .offset:         104
        .size:           4
        .value_kind:     hidden_block_count_z
      - .offset:         108
        .size:           2
        .value_kind:     hidden_group_size_x
      - .offset:         110
        .size:           2
        .value_kind:     hidden_group_size_y
      - .offset:         112
        .size:           2
        .value_kind:     hidden_group_size_z
      - .offset:         114
        .size:           2
        .value_kind:     hidden_remainder_x
      - .offset:         116
        .size:           2
        .value_kind:     hidden_remainder_y
      - .offset:         118
        .size:           2
        .value_kind:     hidden_remainder_z
      - .offset:         136
        .size:           8
        .value_kind:     hidden_global_offset_x
      - .offset:         144
        .size:           8
        .value_kind:     hidden_global_offset_y
      - .offset:         152
        .size:           8
        .value_kind:     hidden_global_offset_z
      - .offset:         160
        .size:           2
        .value_kind:     hidden_grid_dims
      - .offset:         216
        .size:           4
        .value_kind:     hidden_dynamic_lds_size
    .group_segment_fixed_size: 768
    .kernarg_segment_align: 8
    .kernarg_segment_size: 352
    .language:       OpenCL C
    .language_version:
      - 2
      - 0
    .max_flat_workgroup_size: 1024
    .name:           _Z7k_layerILi2EEvPKDF16_PKiPKjS3_S3_S1_PKfPDF16_PhS3_S7_Pf
    .private_segment_fixed_size: 0
    .sgpr_count:     44
    .sgpr_spill_count: 0
    .symbol:         _Z7k_layerILi2EEvPKDF16_PKiPKjS3_S3_S1_PKfPDF16_PhS3_S7_Pf.kd
    .uniform_work_group_size: 1
    .uses_dynamic_stack: false
    .vgpr_count:     102
    .vgpr_spill_count: 0
    .wavefront_size: 64
